# v57 + the MoE gate/up GEMM (P10) K-loop also reads its B operand through ds_read offset immediates (per-trip lane offsets biased by the stage base): all six fp8 GEMM loops now without per-trip address
# speedup vs baseline: 1.0116x; 1.0116x over previous
.LBB0_2471:
	v_and_b32_e32 v0, 15, v4
	v_lshrrev_b32_e32 v2, 3, v4
	v_bfe_u32 v4, v4, 1, 3
	s_mov_b32 s6, 0xffffffe
	v_lshlrev_b32_e32 v0, 7, v0
	v_and_b32_e32 v3, 0xffffffe, v2
	v_bitop3_b32 v2, v2, v4, s6 bitop3:0x6c
	v_or_b32_e32 v1, s64, v0
	v_or_b32_e32 v0, s65, v0
	v_lshlrev_b32_e32 v2, 4, v2
	v_add_u32_e32 v32, v2, v1
	v_add3_u32 v204, v2, v0, s70
	v_bitop3_b32 v2, v3, v4, 1 bitop3:0x36
	v_lshlrev_b32_e32 v2, 4, v2
	v_add3_u32 v205, v2, v0, s70
	v_add_u32_e32 v33, v2, v1
	ds_read_b128 v[16:19], v204 offset:0
	ds_read_b128 v[24:27], v204 offset:2048
	ds_read_b128 v[20:23], v205 offset:0
	ds_read_b128 v[28:31], v205 offset:2048
	ds_read_b128 v[0:3], v204 offset:16384
	ds_read_b128 v[8:11], v204 offset:18432
	ds_read_b128 v[4:7], v205 offset:16384
	ds_read_b128 v[12:15], v205 offset:18432
	s_cmp_eq_u32 s77, 14
	s_cselect_b64 s[6:7], -1, 0
	s_add_i32 s10, s82, 0xffffff00
	s_cmp_lg_u32 s77, 14
	v_add_u32_e32 v200, 0, v32
	s_mov_b32 m0, s66
	v_add_u32_e32 v199, 0, v33
	ds_read_b128 v[40:43], v200
	ds_read_b128 v[32:35], v200 offset:2048
	ds_read_b128 v[44:47], v199
	ds_read_b128 v[36:39], v199 offset:2048
	ds_read_b128 v[56:59], v200 offset:4096
	ds_read_b128 v[48:51], v200 offset:6144
	ds_read_b128 v[60:63], v199 offset:4096
	ds_read_b128 v[52:55], v199 offset:6144
	buffer_load_dwordx4 v66, s[16:19], s10 offen lds
	s_mov_b32 m0, s69
	s_nop 0
	buffer_load_dwordx4 v67, s[16:19], s10 offen lds
	s_cbranch_scc1 .LBB0_2473
	v_add_u32_e32 v64, 0, v206
	v_add_u32_e32 v64, 0x20000, v64
	ds_read_b128 v[64:67], v64
.LBB0_2473:
	v_lshlrev_b32_e32 v206, 1, v203
	v_lshrrev_b32_e32 v207, 2, v203
	s_add_i32 s10, s82, 0xffffff80
	v_and_b32_e32 v206, 24, v206
	v_and_b32_e32 v207, 4, v207
	v_and_b32_e32 v203, 0x1fffe3, v203
	s_waitcnt vmcnt(8)
	s_add_i32 s14, s77, 2
	s_add_i32 s11, s10, s76
	v_or3_b32 v203, v203, v207, v206
	v_lshlrev_b32_e32 v206, 1, v202
	v_lshrrev_b32_e32 v207, 2, v202
	s_waitcnt lgkmcnt(0)
	s_and_b64 s[6:7], s[6:7], exec
	v_and_b32_e32 v206, 24, v206
	v_and_b32_e32 v207, 4, v207
	v_and_b32_e32 v202, 0x1fffe3, v202
	s_cselect_b32 s7, s46, s11
	v_or3_b32 v202, v202, v207, v206
	s_cselect_b32 s6, 0x80, s82
	s_cselect_b32 s83, 0, s10
	s_add_i32 s15, s7, 0x80
	v_lshl_or_b32 v203, v203, 11, v201
	v_lshl_or_b32 v201, v202, 11, v201
	s_barrier
	s_setprio 1
	s_waitcnt lgkmcnt(0)
	v_mfma_f32_16x16x128_f8f6f4 v[192:195], v[16:23], v[40:47], v[192:195]
	v_mfma_f32_16x16x128_f8f6f4 v[188:191], v[24:31], v[40:47], v[188:191]
	v_mfma_f32_16x16x128_f8f6f4 v[176:179], v[16:23], v[32:39], v[176:179]
	v_mfma_f32_16x16x128_f8f6f4 v[168:171], v[24:31], v[32:39], v[168:171]
	v_mfma_f32_16x16x128_f8f6f4 v[160:163], v[16:23], v[56:63], v[160:163]
	v_mfma_f32_16x16x128_f8f6f4 v[152:155], v[24:31], v[56:63], v[152:155]
	v_mfma_f32_16x16x128_f8f6f4 v[144:147], v[16:23], v[48:55], v[144:147]
	v_mfma_f32_16x16x128_f8f6f4 v[136:139], v[24:31], v[48:55], v[136:139]
	s_setprio 0
	s_setprio 1
	v_mfma_f32_16x16x128_f8f6f4 v[184:187], v[0:7], v[40:47], v[184:187]
	v_mfma_f32_16x16x128_f8f6f4 v[180:183], v[8:15], v[40:47], v[180:183]
	v_mfma_f32_16x16x128_f8f6f4 v[172:175], v[0:7], v[32:39], v[172:175]
	v_mfma_f32_16x16x128_f8f6f4 v[164:167], v[8:15], v[32:39], v[164:167]
	v_mfma_f32_16x16x128_f8f6f4 v[156:159], v[0:7], v[56:63], v[156:159]
	v_mfma_f32_16x16x128_f8f6f4 v[148:151], v[8:15], v[56:63], v[148:151]
	v_mfma_f32_16x16x128_f8f6f4 v[140:143], v[0:7], v[48:55], v[140:143]
	v_mfma_f32_16x16x128_f8f6f4 v[132:135], v[8:15], v[48:55], v[132:135]
	s_setprio 0
	s_barrier
	s_mov_b32 m0, s50
	s_mov_b32 s10, s18
	s_mov_b32 s11, s19
	ds_read_b128 v[32:35], v200 offset:16384
	ds_read_b128 v[40:43], v200 offset:18432
	ds_read_b128 v[36:39], v199 offset:16384
	ds_read_b128 v[44:47], v199 offset:18432
	ds_read_b128 v[48:51], v200 offset:20480
	ds_read_b128 v[56:59], v200 offset:22528
	ds_read_b128 v[52:55], v199 offset:20480
	ds_read_b128 v[60:63], v199 offset:22528
	buffer_load_dwordx4 v203, s[8:11], s7 offen lds
	s_mov_b32 m0, s51
	s_add_i32 s84, s7, 0x40000
	buffer_load_dwordx4 v201, s[8:11], s7 offen lds
	s_mov_b32 m0, s52
	s_nop 0
	buffer_load_dwordx4 v203, s[8:11], s84 offen lds
	s_mov_b32 m0, s53
	s_nop 0
	buffer_load_dwordx4 v201, s[8:11], s84 offen lds
	s_mov_b32 m0, s49
	s_nop 0
	buffer_load_dwordx4 v64, s[16:19], s83 offen lds
	s_mov_b32 m0, s54
	s_nop 0
	buffer_load_dwordx4 v65, s[16:19], s83 offen lds
	s_waitcnt vmcnt(8)
	s_waitcnt lgkmcnt(0)
	s_barrier
	s_setprio 1
	s_waitcnt lgkmcnt(5)
	v_mfma_f32_16x16x128_f8f6f4 v[128:131], v[16:23], v[32:39], v[128:131]
	v_mfma_f32_16x16x128_f8f6f4 v[120:123], v[24:31], v[32:39], v[120:123]
	s_waitcnt lgkmcnt(4)
	v_mfma_f32_16x16x128_f8f6f4 v[112:115], v[16:23], v[40:47], v[112:115]
	v_mfma_f32_16x16x128_f8f6f4 v[104:107], v[24:31], v[40:47], v[104:107]
	s_waitcnt lgkmcnt(1)
	v_mfma_f32_16x16x128_f8f6f4 v[96:99], v[16:23], v[48:55], v[96:99]
	v_mfma_f32_16x16x128_f8f6f4 v[88:91], v[24:31], v[48:55], v[88:91]
	s_waitcnt lgkmcnt(0)
	v_mfma_f32_16x16x128_f8f6f4 v[80:83], v[16:23], v[56:63], v[80:83]
	v_mfma_f32_16x16x128_f8f6f4 v[72:75], v[24:31], v[56:63], v[72:75]
	s_setprio 0
	s_setprio 1
	v_mfma_f32_16x16x128_f8f6f4 v[124:127], v[0:7], v[32:39], v[124:127]
	v_mfma_f32_16x16x128_f8f6f4 v[116:119], v[8:15], v[32:39], v[116:119]
	v_mfma_f32_16x16x128_f8f6f4 v[108:111], v[0:7], v[40:47], v[108:111]
	v_mfma_f32_16x16x128_f8f6f4 v[100:103], v[8:15], v[40:47], v[100:103]
	v_mfma_f32_16x16x128_f8f6f4 v[92:95], v[0:7], v[48:55], v[92:95]
	v_mfma_f32_16x16x128_f8f6f4 v[84:87], v[8:15], v[48:55], v[84:87]
	v_mfma_f32_16x16x128_f8f6f4 v[76:79], v[0:7], v[56:63], v[76:79]
	v_mfma_f32_16x16x128_f8f6f4 v[68:71], v[8:15], v[56:63], v[68:71]
	s_setprio 0
	s_barrier
	s_add_i32 s84, 0, 0x18000
	s_add_i32 s84, 0, 0x1c000
	ds_read_b128 v[0:3], v204 offset:32768
	ds_read_b128 v[8:11], v204 offset:34816
	ds_read_b128 v[4:7], v205 offset:32768
	ds_read_b128 v[12:15], v205 offset:34816
	ds_read_b128 v[16:19], v204 offset:49152
	ds_read_b128 v[24:27], v204 offset:51200
	ds_read_b128 v[20:23], v205 offset:49152
	ds_read_b128 v[28:31], v205 offset:51200
	s_mov_b32 m0, s55
	ds_read_b128 v[32:35], v200 offset:32768
	ds_read_b128 v[40:43], v200 offset:34816
	ds_read_b128 v[36:39], v199 offset:32768
	ds_read_b128 v[44:47], v199 offset:34816
	ds_read_b128 v[48:51], v200 offset:36864
	ds_read_b128 v[56:59], v200 offset:38912
	ds_read_b128 v[52:55], v199 offset:36864
	ds_read_b128 v[60:63], v199 offset:38912
	buffer_load_dwordx4 v66, s[16:19], s83 offen lds
	s_mov_b32 m0, s56
	s_nop 0
	buffer_load_dwordx4 v67, s[16:19], s83 offen lds
	s_waitcnt vmcnt(8)
	s_waitcnt lgkmcnt(0)
	s_barrier
	s_setprio 1
	s_waitcnt lgkmcnt(5)
	v_mfma_f32_16x16x128_f8f6f4 v[192:195], v[0:7], v[32:39], v[192:195]
	v_mfma_f32_16x16x128_f8f6f4 v[188:191], v[8:15], v[32:39], v[188:191]
	s_waitcnt lgkmcnt(4)
	v_mfma_f32_16x16x128_f8f6f4 v[176:179], v[0:7], v[40:47], v[176:179]
	v_mfma_f32_16x16x128_f8f6f4 v[168:171], v[8:15], v[40:47], v[168:171]
	s_waitcnt lgkmcnt(1)
	v_mfma_f32_16x16x128_f8f6f4 v[160:163], v[0:7], v[48:55], v[160:163]
	v_mfma_f32_16x16x128_f8f6f4 v[152:155], v[8:15], v[48:55], v[152:155]
	s_waitcnt lgkmcnt(0)
	v_mfma_f32_16x16x128_f8f6f4 v[144:147], v[0:7], v[56:63], v[144:147]
	v_mfma_f32_16x16x128_f8f6f4 v[136:139], v[8:15], v[56:63], v[136:139]
	s_setprio 0
	s_setprio 1
	v_mfma_f32_16x16x128_f8f6f4 v[184:187], v[16:23], v[32:39], v[184:187]
	v_mfma_f32_16x16x128_f8f6f4 v[180:183], v[24:31], v[32:39], v[180:183]
	v_mfma_f32_16x16x128_f8f6f4 v[172:175], v[16:23], v[40:47], v[172:175]
	v_mfma_f32_16x16x128_f8f6f4 v[164:167], v[24:31], v[40:47], v[164:167]
	v_mfma_f32_16x16x128_f8f6f4 v[156:159], v[16:23], v[48:55], v[156:159]
	v_mfma_f32_16x16x128_f8f6f4 v[148:151], v[24:31], v[48:55], v[148:151]
	v_mfma_f32_16x16x128_f8f6f4 v[140:143], v[16:23], v[56:63], v[140:143]
	v_mfma_f32_16x16x128_f8f6f4 v[132:135], v[24:31], v[56:63], v[132:135]
	s_setprio 0
	s_barrier
	s_mov_b32 m0, s58
	ds_read_b128 v[32:35], v200 offset:49152
	ds_read_b128 v[40:43], v200 offset:51200
	ds_read_b128 v[36:39], v199 offset:49152
	ds_read_b128 v[44:47], v199 offset:51200
	ds_read_b128 v[48:51], v200 offset:53248
	ds_read_b128 v[56:59], v200 offset:55296
	ds_read_b128 v[52:55], v199 offset:53248
	ds_read_b128 v[60:63], v199 offset:55296
	buffer_load_dwordx4 v203, s[8:11], s15 offen lds
	s_mov_b32 m0, s59
	s_add_i32 s7, s7, 0x40080
	buffer_load_dwordx4 v201, s[8:11], s15 offen lds
	s_mov_b32 m0, s62
	s_nop 0
	buffer_load_dwordx4 v203, s[8:11], s7 offen lds
	s_mov_b32 m0, s63
	s_nop 0
	buffer_load_dwordx4 v201, s[8:11], s7 offen lds
	s_mov_b32 m0, s60
	s_nop 0
	buffer_load_dwordx4 v64, s[16:19], s6 offen lds
	s_mov_b32 m0, s61
	s_nop 0
	buffer_load_dwordx4 v65, s[16:19], s6 offen lds
	s_waitcnt vmcnt(8)
	s_waitcnt lgkmcnt(0)
	s_barrier
	s_setprio 1
	s_waitcnt lgkmcnt(5)
	v_mfma_f32_16x16x128_f8f6f4 v[128:131], v[0:7], v[32:39], v[128:131]
	v_mfma_f32_16x16x128_f8f6f4 v[120:123], v[8:15], v[32:39], v[120:123]
	s_waitcnt lgkmcnt(4)
	v_mfma_f32_16x16x128_f8f6f4 v[112:115], v[0:7], v[40:47], v[112:115]
	v_mfma_f32_16x16x128_f8f6f4 v[104:107], v[8:15], v[40:47], v[104:107]
	s_waitcnt lgkmcnt(1)
	v_mfma_f32_16x16x128_f8f6f4 v[96:99], v[0:7], v[48:55], v[96:99]
	v_mfma_f32_16x16x128_f8f6f4 v[88:91], v[8:15], v[48:55], v[88:91]
	s_waitcnt lgkmcnt(0)
	v_mfma_f32_16x16x128_f8f6f4 v[80:83], v[0:7], v[56:63], v[80:83]
	v_mfma_f32_16x16x128_f8f6f4 v[72:75], v[8:15], v[56:63], v[72:75]
	s_setprio 0
	s_setprio 1
	v_mfma_f32_16x16x128_f8f6f4 v[124:127], v[16:23], v[32:39], v[124:127]
	v_mfma_f32_16x16x128_f8f6f4 v[116:119], v[24:31], v[32:39], v[116:119]
	v_mfma_f32_16x16x128_f8f6f4 v[108:111], v[16:23], v[40:47], v[108:111]
	v_mfma_f32_16x16x128_f8f6f4 v[100:103], v[24:31], v[40:47], v[100:103]
	v_mfma_f32_16x16x128_f8f6f4 v[92:95], v[16:23], v[48:55], v[92:95]
	v_mfma_f32_16x16x128_f8f6f4 v[84:87], v[24:31], v[48:55], v[84:87]
	v_mfma_f32_16x16x128_f8f6f4 v[76:79], v[16:23], v[56:63], v[76:79]
	v_mfma_f32_16x16x128_f8f6f4 v[68:71], v[24:31], v[56:63], v[68:71]
	s_setprio 0
	s_barrier
	s_addk_i32 s82, 0x100
	s_cmp_gt_u32 s77, 13
	s_cbranch_scc1 .LBB0_2479
	s_mov_b32 s77, s14
	s_branch .LBB0_2454
